# MoE block scheduler table (full blocks round-robin, near-empty blocks dealt separately) replaces L=i*G+c; waves skip MFMA for all-padding row halves
# speedup vs baseline: 1.0020x; 1.0020x over previous
; #define LAS __attribute__((address_space(3)))
;     __device__ __forceinline__ bool next(int i, pg8::Unit& u) const {
;         const int NB = __builtin_amdgcn_readfirstlane(tab[0]); const int L = i * G + c; if (L >= NB * nN) return false;
;         const int b = L / nN, pn = L - b * nN, e = __builtin_amdgcn_readfirstlane(tab[64 + b]);
;         u.pa = A; u.pb = B + (size_t)e * bexp + (size_t)pn * 256 * 128; u.row0 = b * 256; u.col0 = pn * 256; u.aux = e; u.blk = b; return true;
; __device__ __forceinline__ void moe_tables(Ctx& X) {
;     LAS int* tab = (LAS int*)(X.lds + LDS_TAB);
;     if (X.tid < 64) { const int e = X.tid;
;         const int cnt = (e < NE) ? (int)__hip_atomic_load(XP_ctl(X) + CW_CNT + 64 * e, __ATOMIC_RELAXED, __HIP_MEMORY_SCOPE_AGENT) : 0; const int k = (cnt + 255) >> 8;
;         int incl = k;
; #pragma unroll
;         for (int o = 1; o < 64; o <<= 1) { const int t = __shfl_up(incl, o); if (e >= o) incl += t; }
;         const int first = incl - k;
;         if (e < NE) { tab[8 + e] = first; for (int b = 0; b < k; ++b) { if (first + b < MAXBLK) { tab[64 + first + b] = e; tab[256 + first + b] = (cnt - 256 * b) < 256 ? (cnt - 256 * b) : 256; } } }
;         if (e == NE - 1) { tab[8 + NE] = incl; tab[0] = incl < MAXBLK ? incl : MAXBLK; } }
;     __syncthreads();
; }
.LBB0_917:
	s_or_b64 exec, exec, s[8:9]
	s_waitcnt lgkmcnt(0)
	s_barrier
	s_cmp_lg_u32 s93, 0
	s_cbranch_scc1 .Lsch7_done
	s_and_b32 s99, s87, 7
	s_lshr_b32 s101, s87, 3
	s_and_b32 s98, s99, 3
	s_lshl_b32 s98, s98, 2
	s_lshr_b32 s100, s101, 3
	s_or_b32 s98, s98, s100
	s_lshr_b32 s99, s99, 2
	s_lshl_b32 s99, s99, 3
	s_and_b32 s101, s101, 7
	s_or_b32 s101, s101, s99
	s_lshr_b32 s99, s98, 2
	s_and_b32 s100, s98, 3
	s_lshl_b32 s100, s100, 2
	s_or_b32 s99, s99, s100
	v_and_b32_e32 v2, 63, v0
	v_lshlrev_b32_e32 v3, 2, v2
	v_add_u32_e32 v3, 0x23c00, v3
	v_mov_b32_e32 v4, 0x7fff0000
	ds_write_b32 v3, v4
	v_min_u32_e32 v5, 31, v2
	v_lshlrev_b32_e32 v5, 2, v5
	v_add_u32_e32 v5, 0x22020, v5
	ds_read2_b32 v[6:7], v5 offset1:1
	s_waitcnt lgkmcnt(0)
	v_sub_u32_e32 v8, v7, v6
	v_add_u32_e32 v9, -1, v7
	v_max_i32_e32 v9, 0, v9
	v_lshlrev_b32_e32 v9, 2, v9
	v_add_u32_e32 v9, 0x22400, v9
	ds_read_b32 v9, v9
	s_waitcnt lgkmcnt(0)
	v_cmp_gt_i32_e32 vcc, 0x81, v9
	v_cmp_lt_i32_e64 s[10:11], 0, v8
	s_and_b64 vcc, vcc, s[10:11]
	v_cmp_gt_u32_e64 s[10:11], 32, v2
	s_and_b64 vcc, vcc, s[10:11]
	v_cndmask_b32_e64 v10, 0, 1, vcc
	v_cndmask_b32_e64 v8, 0, v8, s[10:11]
	v_sub_u32_e32 v11, v8, v10
	v_lshl_or_b32 v13, v10, 16, v11
	s_nop 1
	v_add_u32_dpp v13, v13, v13 row_shr:1 row_mask:0xf bank_mask:0xf bound_ctrl:0
	s_nop 1
	v_add_u32_dpp v13, v13, v13 row_shr:2 row_mask:0xf bank_mask:0xf bound_ctrl:0
	s_nop 1
	v_add_u32_dpp v13, v13, v13 row_shr:4 row_mask:0xf bank_mask:0xf bound_ctrl:0
	s_nop 1
	v_add_u32_dpp v13, v13, v13 row_shr:8 row_mask:0xf bank_mask:0xf bound_ctrl:0
	s_nop 1
	v_add_u32_dpp v13, v13, v13 row_bcast:15 row_mask:0xa bank_mask:0xf
	s_nop 1
	v_and_b32_e32 v14, 0xffff, v13
	v_sub_u32_e32 v14, v14, v11
	v_lshrrev_b32_e32 v15, 16, v13
	v_sub_u32_e32 v15, v15, v10
	v_add_u32_e32 v16, v14, v11
	v_add_u32_e32 v17, -1, v8
	s_mov_b32 s12, 0
	s_mov_b64 s[8:9], exec
.Lsch7_loop:
	s_mov_b64 exec, s[8:9]
	v_cmp_lt_i32_e32 vcc, s12, v8
	s_and_b64 exec, exec, vcc
	s_cbranch_execz .Lsch7_end
	v_cmp_eq_u32_e32 vcc, s12, v17
	v_cmp_eq_u32_e64 s[10:11], 1, v10
	s_and_b64 vcc, vcc, s[10:11]
	v_add_u32_e32 v3, s12, v14
	v_cndmask_b32_e32 v4, v3, v15, vcc
	v_cndmask_b32_e32 v5, v15, v16, vcc
	v_mov_b32_e32 v7, s98
	v_mov_b32_e32 v9, s99
	v_cndmask_b32_e32 v12, v7, v9, vcc
	v_cndmask_b32_e32 v7, v9, v7, vcc
	v_and_b32_e32 v9, 15, v4
	v_cmp_eq_u32_e32 vcc, v9, v12
	v_lshrrev_b32_e32 v4, 4, v4
	v_add_u32_e32 v5, 15, v5
	v_sub_u32_e32 v5, v5, v7
	v_lshrrev_b32_e32 v5, 4, v5
	v_add_u32_e32 v4, v4, v5
	v_lshlrev_b32_e32 v4, 2, v4
	v_add_u32_e32 v4, 0x23c00, v4
	v_add_u32_e32 v5, s12, v6
	v_lshl_or_b32 v5, v5, 4, s101
	s_and_b64 exec, exec, vcc
	ds_write_b32 v4, v5
	s_add_i32 s12, s12, 1
	s_branch .Lsch7_loop
.Lsch7_end:
	s_mov_b64 exec, s[8:9]
	s_waitcnt lgkmcnt(0)
; #define LAS __attribute__((address_space(3)))
; template <class Epi, class Sched, bool GATHER, bool FP8>
; __device__ __forceinline__ void gemm_phase(LAS uchar* lds, const int K, const int LDA, const int LDB, const size_t kstepA, const size_t kstepB, const Sched& S, const Epi& E) {
;     ...
;     Unit cur, nxt; int ui = 0;
;     if (!S.next(0, cur)) return;
;     f32x4 acc[2][2][4][2];
; #pragma unroll
;     for (int a = 0; a < 2; ++a)
; #pragma unroll
;         for (int b = 0; b < 2; ++b)
; #pragma unroll
;             for (int m = 0; m < 4; ++m)
; #pragma unroll
;                 for (int n = 0; n < 2; ++n) acc[a][b][m][n] = (f32x4){0.f, 0.f, 0.f, 0.f};
;     bf16x8 At[4][2], B0[2][2], B1[2][2];
;     const char* cA = cur.pa; const char* cB = cur.pb;
;     if constexpr (GATHER) S.gather(cur, voA, (const LAS int*)nullptr);
;     __device__ __forceinline__ bool next(int i, pg8::Unit& u) const {
;         const int NB = __builtin_amdgcn_readfirstlane(tab[0]); const int L = i * G + c; if (L >= NB * nN) return false;
;         const int b = L / nN, pn = L - b * nN, e = __builtin_amdgcn_readfirstlane(tab[64 + b]);
;         u.pa = A; u.pb = B + (size_t)e * bexp + (size_t)pn * 256 * 128; u.row0 = b * 256; u.col0 = pn * 256; u.aux = e; u.blk = b; return true;
;     }
;     __device__ __forceinline__ void prefetch(const pg8::Unit& u, LAS uchar* buf, int wid, int lane) const {
;         { const int e = u.aux, lb = (u.blk - __builtin_amdgcn_readfirstlane(tab[8 + e])) * 256, w4 = wid & 3;
;             __builtin_amdgcn_global_load_lds((const unsigned*)(list + e * T + lb + 64 * w4 + lane), (LAS unsigned*)(buf + w4 * 256), 4, 0, 0); }
;     }
;     __device__ __forceinline__ void gather(const pg8::Unit& u, unsigned (&vo)[2][2], const LAS int* idx) const {
;         const int e = u.aux, lb = (u.blk - __builtin_amdgcn_readfirstlane(tab[8 + e])) * 256, cnt = __builtin_amdgcn_readfirstlane(tab[256 + u.blk]);
; #pragma unroll
;         for (int i = 0; i < 2; ++i) { int R, C; pg8::stage_rc((int)threadIdx.x * 16 + i * 8192, R, C);
; #pragma unroll
;             for (int h = 0; h < 2; ++h) { const int r = h * 128 + R; const int raw = idx ? idx[r] : list[e * T + lb + r]; const int tok = (r < cnt) ? raw : 0; vo[h][i] = ((unsigned)tok * (unsigned)K + (unsigned)C) * 2u; } }
;     }
.Lsch7_done:
	s_add_i32 s12, 0, 0x22000
	s_waitcnt vmcnt(4)
	v_mov_b32_e32 v2, s12
	s_waitcnt lgkmcnt(0)
	s_barrier
	ds_read_b32 v2, v2
	v_readfirstlane_b32 s20, v0
	s_waitcnt lgkmcnt(0)
	v_readfirstlane_b32 s2, v2
	s_lshl_b32 s2, s2, 4
	v_mov_b32_e32 v3, 0x23c00
	ds_read_b32 v3, v3
	s_waitcnt lgkmcnt(0)
	v_readfirstlane_b32 s98, v3
	s_cmp_ge_i32 s98, s2
	s_cbranch_scc1 .LBB0_937
	s_add_u32 s8, s90, 0x6000000
	s_addc_u32 s9, s91, 0
	s_add_u32 s25, s90, 0x30000000
	s_addc_u32 s33, s91, 0
	s_add_u32 s10, s90, 0x2f00000
	s_addc_u32 s11, s91, 0
	s_ashr_i32 s2, s98, 31
	s_lshr_b32 s2, s2, 28
	s_add_i32 s2, s98, s2
	s_ashr_i32 s18, s2, 4
	s_lshl_b32 s3, s18, 2
	s_add_i32 s3, s12, s3
	v_mov_b32_e32 v2, s3
	ds_read2st64_b32 v[2:3], v2 offset0:1 offset1:4
	s_lshr_b32 s21, s20, 6
	s_and_b32 s2, s2, -16
	s_lshr_b32 s22, s20, 8
	s_lshl_b32 s52, s21, 10
	s_waitcnt lgkmcnt(0)
	v_readfirstlane_b32 s42, v2
	s_ashr_i32 s43, s42, 31
	s_sub_i32 s2, s98, s2
	s_lshl_b64 s[14:15], s[42:43], 23
	s_add_u32 s13, s25, s14
	s_addc_u32 s16, s33, s15
	s_ashr_i32 s3, s2, 31
	s_lshl_b64 s[14:15], s[2:3], 15
	s_add_u32 s44, s13, s14
	s_addc_u32 s45, s16, s15
	s_lshl_b32 s3, s42, 2
	s_add_i32 s3, s12, s3
	v_mov_b32_e32 v2, s3
	ds_read_b32 v2, v2 offset:32
	v_lshrrev_b32_e32 v13, 3, v0
	v_bfe_u32 v12, v0, 2, 4
	v_or_b32_e32 v4, 64, v13
	s_movk_i32 s3, 0x70
	v_and_or_b32 v195, v4, s3, v12
	s_waitcnt lgkmcnt(0)
	v_readfirstlane_b32 s3, v2
	s_sub_i32 s3, s18, s3
	s_lshl_b32 s3, s3, 8
	s_lshl_b32 s12, s42, 13
	s_add_i32 s3, s3, s12
	v_and_or_b32 v208, v13, 48, v12
	v_or_b32_e32 v4, s3, v208
	v_or_b32_e32 v209, 0x80, v208
	v_or_b32_e32 v210, 0x80, v195
	v_ashrrev_i32_e32 v5, 31, v4
	v_or_b32_e32 v6, s3, v209
	v_or_b32_e32 v8, s3, v195
	v_or_b32_e32 v10, s3, v210
	v_lshl_add_u64 v[4:5], v[4:5], 2, s[10:11]
	v_ashrrev_i32_e32 v7, 31, v6
	v_ashrrev_i32_e32 v9, 31, v8
	v_ashrrev_i32_e32 v11, 31, v10
	v_lshl_add_u64 v[6:7], v[6:7], 2, s[10:11]
	v_lshl_add_u64 v[8:9], v[8:9], 2, s[10:11]
	v_lshl_add_u64 v[10:11], v[10:11], 2, s[10:11]
	global_load_dword v14, v[4:5], off
	global_load_dword v15, v[6:7], off
	global_load_dword v16, v[8:9], off
	global_load_dword v17, v[10:11], off
	v_lshlrev_b32_e32 v4, 4, v0
	v_and_b32_e32 v5, 32, v0
	v_bitop3_b32 v4, v4, v5, 48 bitop3:0x6c
	v_and_or_b32 v5, v13, 32, v12
	v_and_b32_e32 v2, 48, v0
	s_movk_i32 s14, 0x46
	v_and_or_b32 v211, v0, 64, v4
	v_lshlrev_b32_e32 v4, 1, v5
	s_movk_i32 s3, 0xc6
	v_lshlrev_b32_e32 v5, 1, v195
	v_and_or_b32 v4, v4, s14, v2
	s_add_i32 s53, s52, 0
	v_and_b32_e32 v6, 0x80, v0
	v_mov_b32_e32 v197, 0
	v_and_or_b32 v5, v5, s3, v2
	v_lshlrev_b32_e32 v4, 7, v4
	s_add_i32 s54, s53, 0x10000
	v_mov_b32_e32 v199, v197
	v_lshlrev_b32_e32 v5, 7, v5
	v_or3_b32 v198, v4, v6, v211
	s_add_i32 s55, s53, 0x12000
	s_mov_b32 m0, s54
	s_mov_b64 s[12:13], 0x400
	v_or3_b32 v200, v5, v6, v211
	v_readfirstlane_b32 s3, v3
	v_lshl_add_u64 v[4:5], s[44:45], 0, v[198:199]
	s_add_i32 s56, s53, 0x14000
	global_load_lds_dwordx4 v198, s[44:45]
	s_mov_b32 m0, s55
	v_mov_b32_e32 v201, v197
	v_lshl_add_u64 v[4:5], v[4:5], 0, s[12:13]
	global_load_lds_dwordx4 v200, s[44:45]
	s_mov_b32 m0, s56
	v_cmp_gt_i32_e32 vcc, s3, v208
	v_lshl_add_u64 v[6:7], s[44:45], 0, v[200:201]
	s_add_i32 s57, s53, 0x16000
	global_load_lds_dwordx4 v[4:5], off
	v_lshl_add_u64 v[6:7], v[6:7], 0, s[12:13]
	s_mov_b32 m0, s57
	s_add_i32 s58, s53, 0x2000
	global_load_lds_dwordx4 v[6:7], off
	s_mov_b32 m0, s53
	s_add_i32 s59, s53, 0x4000
	s_add_i32 s60, s53, 0x6000
	s_load_dwordx2 s[14:15], s[0:1], 0x78
	s_cmp_eq_u32 s22, 1
	s_mov_b32 s46, 0
	s_cselect_b64 s[16:17], -1, 0
	s_cmp_lg_u32 s22, 1
	v_mov_b32_e32 v203, v197
	s_waitcnt vmcnt(0)
	v_mul_u32_u24_e32 v3, 0x880, v14
	v_mul_u32_u24_e32 v4, 0x880, v15
	v_cndmask_b32_e32 v3, 0, v3, vcc
	v_cmp_gt_i32_e32 vcc, s3, v209
	v_mul_u32_u24_e32 v5, 0x880, v16
	v_or_b32_e32 v196, v3, v211
	v_cndmask_b32_e32 v4, 0, v4, vcc
	v_cmp_gt_i32_e32 vcc, s3, v195
	v_mul_u32_u24_e32 v6, 0x880, v17
	global_load_lds_dwordx4 v196, s[8:9]
	v_cndmask_b32_e32 v5, 0, v5, vcc
	v_cmp_gt_i32_e32 vcc, s3, v210
	v_or_b32_e32 v202, v5, v211
	s_mov_b32 m0, s58
	v_cndmask_b32_e32 v6, 0, v6, vcc
	v_or_b32_e32 v3, v4, v211
	global_load_lds_dwordx4 v202, s[8:9]
	s_mov_b32 m0, s59
	v_or_b32_e32 v204, v6, v211
	global_load_lds_dwordx4 v3, s[8:9]
	s_mov_b32 m0, s60
	s_nop 0
	global_load_lds_dwordx4 v204, s[8:9]
	s_cbranch_scc1 .LBB0_920
	s_barrier

; template <class Epi, class Sched, bool GATHER, bool FP8>
; __device__ __forceinline__ void gemm_phase(LAS uchar* lds, const int K, const int LDA, const int LDB, const size_t kstepA, const size_t kstepB, const Sched& S, const Epi& E) {
;     ...
;         const bool has_next = S.next(ui + 1, nxt);
;         if constexpr (GATHER) { if (has_next) S.prefetch(nxt, lds + LDS_IDX + ((ui + 1) & 1) * 1024, wid, lane); }
;         E.prefetch(cur, lds + LDS_BIAS + (ui & 1) * 1024, wid, lane);
;         const char* nA = has_next ? nxt.pa : cA; const char* nB = has_next ? nxt.pb : cB;
;     __device__ __forceinline__ bool next(int i, pg8::Unit& u) const {
;         const int NB = __builtin_amdgcn_readfirstlane(tab[0]); const int L = i * G + c; if (L >= NB * nN) return false;
;         const int b = L / nN, pn = L - b * nN, e = __builtin_amdgcn_readfirstlane(tab[64 + b]);
;         u.pa = A; u.pb = B + (size_t)e * bexp + (size_t)pn * 256 * 128; u.row0 = b * 256; u.col0 = pn * 256; u.aux = e; u.blk = b; return true;
.LBB0_923:
	s_lshr_b32 s99, s73, 6
	s_add_i32 s99, s99, 0x22400
	v_mov_b32_e32 v250, s99
	ds_read_b32 v250, v250
	s_lshr_b32 s101, s93, 2
	s_lshl_b32 s101, s101, 6
	s_waitcnt lgkmcnt(0)
	v_readfirstlane_b32 s99, v250
	s_cmp_le_i32 s99, s101
	s_cselect_b32 s100, 1, 0
	s_add_i32 s101, s101, 0x80
	s_cmp_le_i32 s99, s101
	s_cselect_b32 s99, 2, 0
	s_or_b32 s99, s99, s100
	ds_read_b32 v2, v213
	s_add_i32 s71, s46, 1
	s_lshl_b32 s2, s71, 2
	s_add_i32 s2, s2, 0x23c00
	v_mov_b32_e32 v249, s2
	ds_read_b32 v249, v249
	s_waitcnt lgkmcnt(0)
	v_readfirstlane_b32 s3, v2
	s_lshl_b32 s3, s3, 4
	v_readfirstlane_b32 s2, v249
	s_cmp_lt_i32 s2, s3
	s_cselect_b64 s[40:41], -1, 0
	s_cmp_ge_i32 s2, s3
	s_cbranch_scc1 .LBB0_925
	s_ashr_i32 s3, s2, 31
	s_lshr_b32 s3, s3, 28
	s_add_i32 s3, s2, s3
	s_ashr_i32 s70, s3, 4
	s_lshl_b32 s26, s70, 2
	s_add_i32 s26, s26, 0
	s_add_i32 s26, s26, 0x22100
	v_mov_b32_e32 v2, s26
	ds_read_b32 v2, v2
	s_and_b32 s3, s3, -16
	s_sub_i32 s2, s2, s3
	s_waitcnt lgkmcnt(0)
	v_readfirstlane_b32 s26, v2
	s_ashr_i32 s27, s26, 31
	s_lshl_b64 s[28:29], s[26:27], 23
	s_add_u32 s27, s25, s28
	s_addc_u32 s30, s33, s29
	s_ashr_i32 s3, s2, 31
	s_lshl_b64 s[28:29], s[2:3], 15
	s_add_u32 s28, s27, s28
	s_addc_u32 s29, s30, s29
	s_lshl_b32 s72, s70, 8
	s_lshl_b32 s27, s2, 8

; #define PG8_STAGE(bufoff, gbase, voff) do { _Pragma("unroll") for (int _i = 0; _i < 2; ++_i) \
;         __builtin_amdgcn_global_load_lds((const unsigned*)((const char*)(gbase) + (voff)[_i]), (LAS unsigned*)(lds + (bufoff) + ldsw + _i * 8192), 16, 0, 0); } while (0)
; #define PG8_LDA(dst, b, h) do { _Pragma("unroll") for (int m = 0; m < 4; ++m) _Pragma("unroll") for (int k = 0; k < 2; ++k) dst[m][k] = *(const LAS bf16x8*)(lds + PG8_SA(b, h) + aoff + m * 2048 + k * 1024); } while (0)
; #define PG8_WAIT_V8F(fresh) asm volatile("s_cmp_eq_u32 %0, 0\n\ts_cbranch_scc1 .Lw8_%=\n\ts_waitcnt vmcnt(%1)\n\ts_branch .Lwe_%=\n.Lw8_%=:\n\ts_waitcnt vmcnt(8)\n.Lwe_%=:" :: "s"(fresh), "n"(8 + Epi::NST + Epi::NPF) : "memory", "scc")
; #define PG8_WAIT_L(n) asm volatile("s_waitcnt lgkmcnt(" #n ")" ::: "memory")
; #define PG8_BAR __builtin_amdgcn_s_barrier()
; #define PG8_SCHED __builtin_amdgcn_sched_barrier(0)
; template <class Epi, class Sched, bool GATHER, bool FP8>
; __device__ __forceinline__ void gemm_phase(LAS uchar* lds, const int K, const int LDA, const int LDB, const size_t kstepA, const size_t kstepB, const Sched& S, const Epi& E) {
;     ...
;             PG8_WAIT_V8F(fresh); PG8_WAIT_L(0); PG8_BAR; PG8_MMA(0, 0, At, B0); PG8_MMA(0, 1, At, B1); PG8_BAR; PG8_SCHED;
;             PG8_LDA(At, 0, 1); PG8_STAGE(PG8_SB(0, 0), b2, voffB); PG8_STAGE(PG8_SB(0, 1), b2 + hstep, voffB); PG8_STAGE(PG8_SA(0, 0), a2, voA[0]);
.Lwe_4:
	s_waitcnt lgkmcnt(0)
	s_barrier
	s_setprio 1
	s_waitcnt lgkmcnt(0)
	s_bitcmp1_b32 s99, 0
	s_cbranch_scc1 .Lmsk7_0
	v_mfma_scale_f32_16x16x128_f8f6f4 v[190:193], v[18:25], v[58:65], v[190:193], v218, v218 op_sel_hi:[0,0,0]
	v_mfma_scale_f32_16x16x128_f8f6f4 v[186:189], v[26:33], v[58:65], v[186:189], v218, v218 op_sel_hi:[0,0,0]
	v_mfma_scale_f32_16x16x128_f8f6f4 v[174:177], v[18:25], v[50:57], v[174:177], v218, v218 op_sel_hi:[0,0,0]
	v_mfma_scale_f32_16x16x128_f8f6f4 v[170:173], v[26:33], v[50:57], v[170:173], v218, v218 op_sel_hi:[0,0,0]
	v_mfma_scale_f32_16x16x128_f8f6f4 v[158:161], v[18:25], v[42:49], v[158:161], v218, v218 op_sel_hi:[0,0,0]
	v_mfma_scale_f32_16x16x128_f8f6f4 v[154:157], v[26:33], v[42:49], v[154:157], v218, v218 op_sel_hi:[0,0,0]
	v_mfma_scale_f32_16x16x128_f8f6f4 v[142:145], v[18:25], v[34:41], v[142:145], v218, v218 op_sel_hi:[0,0,0]
	v_mfma_scale_f32_16x16x128_f8f6f4 v[138:141], v[26:33], v[34:41], v[138:141], v218, v218 op_sel_hi:[0,0,0]
	s_setprio 0
	s_setprio 1
	v_mfma_scale_f32_16x16x128_f8f6f4 v[182:185], v[2:9], v[58:65], v[182:185], v218, v218 op_sel_hi:[0,0,0]
	v_mfma_scale_f32_16x16x128_f8f6f4 v[178:181], v[10:17], v[58:65], v[178:181], v218, v218 op_sel_hi:[0,0,0]
	v_mfma_scale_f32_16x16x128_f8f6f4 v[166:169], v[2:9], v[50:57], v[166:169], v218, v218 op_sel_hi:[0,0,0]
	v_mfma_scale_f32_16x16x128_f8f6f4 v[162:165], v[10:17], v[50:57], v[162:165], v218, v218 op_sel_hi:[0,0,0]
	v_mfma_scale_f32_16x16x128_f8f6f4 v[150:153], v[2:9], v[42:49], v[150:153], v218, v218 op_sel_hi:[0,0,0]
	v_mfma_scale_f32_16x16x128_f8f6f4 v[146:149], v[10:17], v[42:49], v[146:149], v218, v218 op_sel_hi:[0,0,0]
	v_mfma_scale_f32_16x16x128_f8f6f4 v[134:137], v[2:9], v[34:41], v[134:137], v218, v218 op_sel_hi:[0,0,0]
	v_mfma_scale_f32_16x16x128_f8f6f4 v[130:133], v[10:17], v[34:41], v[130:133], v218, v218 op_sel_hi:[0,0,0]
.Lmsk7_0:
	s_setprio 0
	s_barrier
	s_mov_b32 m0, s54
	v_lshl_add_u64 v[222:223], s[46:47], 0, v[198:199]
	ds_read_b128 v[34:37], v217 offset:16384
	ds_read_b128 v[38:41], v217 offset:17408
	ds_read_b128 v[42:45], v217 offset:18432
	ds_read_b128 v[46:49], v217 offset:19456
	ds_read_b128 v[50:53], v217 offset:20480
	ds_read_b128 v[54:57], v217 offset:21504
	ds_read_b128 v[58:61], v217 offset:22528
	ds_read_b128 v[62:65], v217 offset:23552
	global_load_lds_dwordx4 v[222:223], off
	v_lshl_add_u64 v[224:225], s[46:47], 0, v[200:201]
	s_mov_b32 m0, s55
	v_lshl_add_u64 v[222:223], v[222:223], 0, s[12:13]
	global_load_lds_dwordx4 v[224:225], off
	s_mov_b32 m0, s56
	v_mov_b32_e32 v207, v197
	global_load_lds_dwordx4 v[222:223], off
	v_lshl_add_u64 v[222:223], v[224:225], 0, s[12:13]
	s_mov_b32 m0, s57
	v_mov_b32_e32 v203, v197
	global_load_lds_dwordx4 v[222:223], off
	s_mov_b32 m0, s53
	v_lshl_add_u64 v[222:223], s[50:51], 0, v[206:207]
	global_load_lds_dwordx4 v206, s[50:51]
	s_mov_b32 m0, s58
	v_lshl_add_u64 v[224:225], s[50:51], 0, v[202:203]
	global_load_lds_dwordx4 v202, s[50:51]
	s_cmp_eq_u32 s78, 0
	s_cbranch_scc1 .Lw8_5
	s_waitcnt vmcnt(17)
	s_branch .Lwe_5

; #define PG8_STAGE(bufoff, gbase, voff) do { _Pragma("unroll") for (int _i = 0; _i < 2; ++_i) \
;         __builtin_amdgcn_global_load_lds((const unsigned*)((const char*)(gbase) + (voff)[_i]), (LAS unsigned*)(lds + (bufoff) + ldsw + _i * 8192), 16, 0, 0); } while (0)
; #define PG8_LDA(dst, b, h) do { _Pragma("unroll") for (int m = 0; m < 4; ++m) _Pragma("unroll") for (int k = 0; k < 2; ++k) dst[m][k] = *(const LAS bf16x8*)(lds + PG8_SA(b, h) + aoff + m * 2048 + k * 1024); } while (0)
; #define PG8_LDB(dst, b, h) do { _Pragma("unroll") for (int n = 0; n < 2; ++n) _Pragma("unroll") for (int k = 0; k < 2; ++k) dst[n][k] = *(const LAS bf16x8*)(lds + PG8_SB(b, h) + boff + n * 2048 + k * 1024); } while (0)
; #define PG8_WAIT_V(n) asm volatile("s_waitcnt vmcnt(" #n ")" ::: "memory")
; #define PG8_WAIT_V8F(fresh) asm volatile("s_cmp_eq_u32 %0, 0\n\ts_cbranch_scc1 .Lw8_%=\n\ts_waitcnt vmcnt(%1)\n\ts_branch .Lwe_%=\n.Lw8_%=:\n\ts_waitcnt vmcnt(8)\n.Lwe_%=:" :: "s"(fresh), "n"(8 + Epi::NST + Epi::NPF) : "memory", "scc")
; #define PG8_WAIT_L(n) asm volatile("s_waitcnt lgkmcnt(" #n ")" ::: "memory")
; #define PG8_BAR __builtin_amdgcn_s_barrier()
; #define PG8_SCHED __builtin_amdgcn_sched_barrier(0)
; template <class Epi, class Sched, bool GATHER, bool FP8>
; __device__ __forceinline__ void gemm_phase(LAS uchar* lds, const int K, const int LDA, const int LDB, const size_t kstepA, const size_t kstepB, const Sched& S, const Epi& E) {
;     ...
;             PG8_WAIT_V8F(fresh); PG8_WAIT_L(0); PG8_BAR; PG8_MMA(1, 0, At, B0); PG8_MMA(1, 1, At, B1); PG8_BAR; PG8_SCHED;
;             PG8_LDB(B0, 1, 0); PG8_LDB(B1, 1, 1); PG8_SCHED; PG8_LDA(At, 1, 0); PG8_STAGE(PG8_SA(0, 1), a2, voA[1]);
;             PG8_WAIT_V(8); PG8_WAIT_L(0); PG8_BAR; PG8_MMA(0, 0, At, B0); PG8_MMA(0, 1, At, B1); PG8_BAR; PG8_SCHED;
.Lwe_5:
	s_waitcnt lgkmcnt(0)
	s_barrier
	s_setprio 1
	s_waitcnt lgkmcnt(0)
	s_bitcmp1_b32 s99, 1
	s_cbranch_scc1 .Lmsk7_1
	v_mfma_scale_f32_16x16x128_f8f6f4 v[126:129], v[18:25], v[34:41], v[126:129], v218, v218 op_sel_hi:[0,0,0]
	v_mfma_scale_f32_16x16x128_f8f6f4 v[122:125], v[26:33], v[34:41], v[122:125], v218, v218 op_sel_hi:[0,0,0]
	v_mfma_scale_f32_16x16x128_f8f6f4 v[110:113], v[18:25], v[42:49], v[110:113], v218, v218 op_sel_hi:[0,0,0]
	v_mfma_scale_f32_16x16x128_f8f6f4 v[106:109], v[26:33], v[42:49], v[106:109], v218, v218 op_sel_hi:[0,0,0]
	v_mfma_scale_f32_16x16x128_f8f6f4 v[94:97], v[18:25], v[50:57], v[94:97], v218, v218 op_sel_hi:[0,0,0]
	v_mfma_scale_f32_16x16x128_f8f6f4 v[90:93], v[26:33], v[50:57], v[90:93], v218, v218 op_sel_hi:[0,0,0]
	v_mfma_scale_f32_16x16x128_f8f6f4 v[78:81], v[18:25], v[58:65], v[78:81], v218, v218 op_sel_hi:[0,0,0]
	v_mfma_scale_f32_16x16x128_f8f6f4 v[74:77], v[26:33], v[58:65], v[74:77], v218, v218 op_sel_hi:[0,0,0]
	s_setprio 0
	s_setprio 1
	v_mfma_scale_f32_16x16x128_f8f6f4 v[118:121], v[2:9], v[34:41], v[118:121], v218, v218 op_sel_hi:[0,0,0]
	v_mfma_scale_f32_16x16x128_f8f6f4 v[114:117], v[10:17], v[34:41], v[114:117], v218, v218 op_sel_hi:[0,0,0]
	v_mfma_scale_f32_16x16x128_f8f6f4 v[102:105], v[2:9], v[42:49], v[102:105], v218, v218 op_sel_hi:[0,0,0]
	v_mfma_scale_f32_16x16x128_f8f6f4 v[98:101], v[10:17], v[42:49], v[98:101], v218, v218 op_sel_hi:[0,0,0]
	v_mfma_scale_f32_16x16x128_f8f6f4 v[86:89], v[2:9], v[50:57], v[86:89], v218, v218 op_sel_hi:[0,0,0]
	v_mfma_scale_f32_16x16x128_f8f6f4 v[82:85], v[10:17], v[50:57], v[82:85], v218, v218 op_sel_hi:[0,0,0]
	v_mfma_scale_f32_16x16x128_f8f6f4 v[70:73], v[2:9], v[58:65], v[70:73], v218, v218 op_sel_hi:[0,0,0]
	v_mfma_scale_f32_16x16x128_f8f6f4 v[66:69], v[10:17], v[58:65], v[66:69], v218, v218 op_sel_hi:[0,0,0]
.Lmsk7_1:
	s_setprio 0
	s_barrier
	s_add_i32 s78, 0, 0x18000
	s_add_i32 s79, 0, 0x1c000
	v_add_u32_e32 v14, s78, v212
	v_add_u32_e32 v30, s79, v212
	ds_read_b128 v[2:5], v14
	ds_read_b128 v[6:9], v14 offset:1024
	ds_read_b128 v[10:13], v14 offset:2048
	ds_read_b128 v[14:17], v14 offset:3072
	ds_read_b128 v[18:21], v30
	ds_read_b128 v[22:25], v30 offset:1024
	ds_read_b128 v[26:29], v30 offset:2048
	ds_read_b128 v[30:33], v30 offset:3072
	s_mov_b32 m0, s59
	v_lshl_add_u64 v[226:227], s[50:51], 0, v[196:197]
	ds_read_b128 v[34:37], v217 offset:32768
	ds_read_b128 v[38:41], v217 offset:33792
	ds_read_b128 v[42:45], v217 offset:34816
	ds_read_b128 v[46:49], v217 offset:35840
	ds_read_b128 v[50:53], v217 offset:36864
	ds_read_b128 v[54:57], v217 offset:37888
	ds_read_b128 v[58:61], v217 offset:38912
	ds_read_b128 v[62:65], v217 offset:39936
	global_load_lds_dwordx4 v[226:227], off
	v_lshl_add_u64 v[226:227], s[50:51], 0, v[204:205]
	s_mov_b32 m0, s60
	s_nop 0
	global_load_lds_dwordx4 v[226:227], off
	s_waitcnt vmcnt(8)
	s_waitcnt lgkmcnt(0)
	s_barrier
	s_setprio 1
	s_waitcnt lgkmcnt(0)
	s_bitcmp1_b32 s99, 0
	s_cbranch_scc1 .Lmsk7_2
	v_mfma_scale_f32_16x16x128_f8f6f4 v[190:193], v[2:9], v[34:41], v[190:193], v218, v218 op_sel_hi:[0,0,0]
	v_mfma_scale_f32_16x16x128_f8f6f4 v[186:189], v[10:17], v[34:41], v[186:189], v218, v218 op_sel_hi:[0,0,0]
	v_mfma_scale_f32_16x16x128_f8f6f4 v[174:177], v[2:9], v[42:49], v[174:177], v218, v218 op_sel_hi:[0,0,0]
	v_mfma_scale_f32_16x16x128_f8f6f4 v[170:173], v[10:17], v[42:49], v[170:173], v218, v218 op_sel_hi:[0,0,0]
	v_mfma_scale_f32_16x16x128_f8f6f4 v[158:161], v[2:9], v[50:57], v[158:161], v218, v218 op_sel_hi:[0,0,0]
	v_mfma_scale_f32_16x16x128_f8f6f4 v[154:157], v[10:17], v[50:57], v[154:157], v218, v218 op_sel_hi:[0,0,0]
	v_mfma_scale_f32_16x16x128_f8f6f4 v[142:145], v[2:9], v[58:65], v[142:145], v218, v218 op_sel_hi:[0,0,0]
	v_mfma_scale_f32_16x16x128_f8f6f4 v[138:141], v[10:17], v[58:65], v[138:141], v218, v218 op_sel_hi:[0,0,0]
	s_setprio 0
	s_setprio 1
	v_mfma_scale_f32_16x16x128_f8f6f4 v[182:185], v[18:25], v[34:41], v[182:185], v218, v218 op_sel_hi:[0,0,0]
	v_mfma_scale_f32_16x16x128_f8f6f4 v[178:181], v[26:33], v[34:41], v[178:181], v218, v218 op_sel_hi:[0,0,0]
	v_mfma_scale_f32_16x16x128_f8f6f4 v[166:169], v[18:25], v[42:49], v[166:169], v218, v218 op_sel_hi:[0,0,0]
	v_mfma_scale_f32_16x16x128_f8f6f4 v[162:165], v[26:33], v[42:49], v[162:165], v218, v218 op_sel_hi:[0,0,0]
	v_mfma_scale_f32_16x16x128_f8f6f4 v[150:153], v[18:25], v[50:57], v[150:153], v218, v218 op_sel_hi:[0,0,0]
	v_mfma_scale_f32_16x16x128_f8f6f4 v[146:149], v[26:33], v[50:57], v[146:149], v218, v218 op_sel_hi:[0,0,0]
	v_mfma_scale_f32_16x16x128_f8f6f4 v[134:137], v[18:25], v[58:65], v[134:137], v218, v218 op_sel_hi:[0,0,0]
	v_mfma_scale_f32_16x16x128_f8f6f4 v[130:133], v[26:33], v[58:65], v[130:133], v218, v218 op_sel_hi:[0,0,0]
; #define PG8_STAGE(bufoff, gbase, voff) do { _Pragma("unroll") for (int _i = 0; _i < 2; ++_i) \
;         __builtin_amdgcn_global_load_lds((const unsigned*)((const char*)(gbase) + (voff)[_i]), (LAS unsigned*)(lds + (bufoff) + ldsw + _i * 8192), 16, 0, 0); } while (0)
; #define PG8_LDA(dst, b, h) do { _Pragma("unroll") for (int m = 0; m < 4; ++m) _Pragma("unroll") for (int k = 0; k < 2; ++k) dst[m][k] = *(const LAS bf16x8*)(lds + PG8_SA(b, h) + aoff + m * 2048 + k * 1024); } while (0)
; #define PG8_WAIT_V(n) asm volatile("s_waitcnt vmcnt(" #n ")" ::: "memory")
; #define PG8_WAIT_L(n) asm volatile("s_waitcnt lgkmcnt(" #n ")" ::: "memory")
; #define PG8_BAR __builtin_amdgcn_s_barrier()
; #define PG8_SCHED __builtin_amdgcn_sched_barrier(0)
; template <class Epi, class Sched, bool GATHER, bool FP8>
; __device__ __forceinline__ void gemm_phase(LAS uchar* lds, const int K, const int LDA, const int LDB, const size_t kstepA, const size_t kstepB, const Sched& S, const Epi& E) {
;     ...
;             PG8_WAIT_V(8); PG8_WAIT_L(0); PG8_BAR; PG8_MMA(0, 0, At, B0); PG8_MMA(0, 1, At, B1); PG8_BAR; PG8_SCHED;
;             PG8_LDA(At, 1, 1); PG8_STAGE(PG8_SB(1, 0), b3, voffB); PG8_STAGE(PG8_SB(1, 1), b3 + hstep, voffB); PG8_STAGE(PG8_SA(1, 0), a3, voA[0]);
;             PG8_WAIT_V(8); PG8_WAIT_L(0); PG8_BAR; PG8_MMA(1, 0, At, B0); PG8_MMA(1, 1, At, B1); PG8_BAR; PG8_SCHED;
.Lmsk7_2:
	s_setprio 0
	s_barrier
	s_add_i32 s50, s78, s52
	v_lshl_add_u64 v[226:227], s[48:49], 0, v[198:199]
	s_mov_b32 m0, s50
	ds_read_b128 v[34:37], v217 offset:49152
	ds_read_b128 v[38:41], v217 offset:50176
	ds_read_b128 v[42:45], v217 offset:51200
	ds_read_b128 v[46:49], v217 offset:52224
	ds_read_b128 v[50:53], v217 offset:53248
	ds_read_b128 v[54:57], v217 offset:54272
	ds_read_b128 v[58:61], v217 offset:55296
	ds_read_b128 v[62:65], v217 offset:56320
	global_load_lds_dwordx4 v[226:227], off
	s_add_i32 m0, s50, 0x2000
	s_add_u32 s46, s46, 0x80400
	v_lshl_add_u64 v[226:227], s[48:49], 0, v[200:201]
	s_addc_u32 s47, s47, 0
	s_add_i32 s48, s79, s52
	global_load_lds_dwordx4 v[226:227], off
	v_lshl_add_u64 v[226:227], s[46:47], 0, v[198:199]
	s_mov_b32 m0, s48
	v_lshl_add_u64 v[222:223], v[222:223], 0, s[22:23]
	global_load_lds_dwordx4 v[226:227], off
	v_lshl_add_u64 v[226:227], s[46:47], 0, v[200:201]
	s_add_i32 m0, s48, 0x2000
	s_nop 0
	global_load_lds_dwordx4 v[226:227], off
	s_mov_b32 m0, s62
	s_nop 0
	global_load_lds_dwordx4 v[222:223], off
	v_lshl_add_u64 v[222:223], v[224:225], 0, s[22:23]
	s_mov_b32 m0, s63
	s_nop 0
	global_load_lds_dwordx4 v[222:223], off
	s_waitcnt vmcnt(8)
	s_waitcnt lgkmcnt(0)
	s_barrier
	s_setprio 1
	s_waitcnt lgkmcnt(0)
	s_bitcmp1_b32 s99, 1
	s_cbranch_scc1 .Lmsk7_3
	v_mfma_scale_f32_16x16x128_f8f6f4 v[126:129], v[2:9], v[34:41], v[126:129], v218, v218 op_sel_hi:[0,0,0]
	v_mfma_scale_f32_16x16x128_f8f6f4 v[122:125], v[10:17], v[34:41], v[122:125], v218, v218 op_sel_hi:[0,0,0]
	v_mfma_scale_f32_16x16x128_f8f6f4 v[110:113], v[2:9], v[42:49], v[110:113], v218, v218 op_sel_hi:[0,0,0]
	v_mfma_scale_f32_16x16x128_f8f6f4 v[106:109], v[10:17], v[42:49], v[106:109], v218, v218 op_sel_hi:[0,0,0]
	v_mfma_scale_f32_16x16x128_f8f6f4 v[94:97], v[2:9], v[50:57], v[94:97], v218, v218 op_sel_hi:[0,0,0]
	v_mfma_scale_f32_16x16x128_f8f6f4 v[90:93], v[10:17], v[50:57], v[90:93], v218, v218 op_sel_hi:[0,0,0]
	v_mfma_scale_f32_16x16x128_f8f6f4 v[78:81], v[2:9], v[58:65], v[78:81], v218, v218 op_sel_hi:[0,0,0]
	v_mfma_scale_f32_16x16x128_f8f6f4 v[74:77], v[10:17], v[58:65], v[74:77], v218, v218 op_sel_hi:[0,0,0]
	s_setprio 0
	s_setprio 1
	v_mfma_scale_f32_16x16x128_f8f6f4 v[118:121], v[18:25], v[34:41], v[118:121], v218, v218 op_sel_hi:[0,0,0]
	v_mfma_scale_f32_16x16x128_f8f6f4 v[114:117], v[26:33], v[34:41], v[114:117], v218, v218 op_sel_hi:[0,0,0]
	v_mfma_scale_f32_16x16x128_f8f6f4 v[102:105], v[18:25], v[42:49], v[102:105], v218, v218 op_sel_hi:[0,0,0]
	v_mfma_scale_f32_16x16x128_f8f6f4 v[98:101], v[26:33], v[42:49], v[98:101], v218, v218 op_sel_hi:[0,0,0]
	v_mfma_scale_f32_16x16x128_f8f6f4 v[86:89], v[18:25], v[50:57], v[86:89], v218, v218 op_sel_hi:[0,0,0]
	v_mfma_scale_f32_16x16x128_f8f6f4 v[82:85], v[26:33], v[50:57], v[82:85], v218, v218 op_sel_hi:[0,0,0]
	v_mfma_scale_f32_16x16x128_f8f6f4 v[70:73], v[18:25], v[58:65], v[70:73], v218, v218 op_sel_hi:[0,0,0]
	v_mfma_scale_f32_16x16x128_f8f6f4 v[66:69], v[26:33], v[58:65], v[66:69], v218, v218 op_sel_hi:[0,0,0]
.Lmsk7_3:
	s_setprio 0
	s_barrier
	s_add_i32 s77, s77, 2
	s_add_u32 s44, s44, 0x100
	s_addc_u32 s45, s45, 0
	s_add_u32 s75, s75, 0x100000
	s_addc_u32 s76, s76, 0
	s_cmp_gt_u32 s77, 13
	s_cbranch_scc1 .LBB0_931

; #define LAS __attribute__((address_space(3)))
;     __device__ __forceinline__ bool next(int i, pg8::Unit& u) const {
;         const int NB = __builtin_amdgcn_readfirstlane(tab[0]); const int L = i * G + c; if (L >= NB * nN) return false;
;         const int b = L / nN, pn = L - b * nN, e = __builtin_amdgcn_readfirstlane(tab[64 + b]);
;         u.pa = A; u.pb = B + (size_t)e * bexp + (size_t)pn * 256 * 128; u.row0 = b * 256; u.col0 = pn * 256; u.aux = e; u.blk = b; return true;
; __device__ __forceinline__ void moe_tables(Ctx& X) {
;     LAS int* tab = (LAS int*)(X.lds + LDS_TAB);
;     if (X.tid < 64) { const int e = X.tid;
;         const int cnt = (e < NE) ? (int)__hip_atomic_load(XP_ctl(X) + CW_CNT + 64 * e, __ATOMIC_RELAXED, __HIP_MEMORY_SCOPE_AGENT) : 0; const int k = (cnt + 255) >> 8;
;         int incl = k;
; #pragma unroll
;         for (int o = 1; o < 64; o <<= 1) { const int t = __shfl_up(incl, o); if (e >= o) incl += t; }
;         const int first = incl - k;
;         if (e < NE) { tab[8 + e] = first; for (int b = 0; b < k; ++b) { if (first + b < MAXBLK) { tab[64 + first + b] = e; tab[256 + first + b] = (cnt - 256 * b) < 256 ? (cnt - 256 * b) : 256; } } }
;         if (e == NE - 1) { tab[8 + NE] = incl; tab[0] = incl < MAXBLK ? incl : MAXBLK; } }
;     __syncthreads();
; }
.LBB0_1022:
	s_cmp_lg_u32 s93, 0
	s_cbranch_scc1 .Lsch8_done
	s_and_b32 s98, s87, 7
	s_lshl_b32 s98, s98, 2
	s_lshr_b32 s100, s87, 6
	s_or_b32 s98, s98, s100
	s_bfe_u32 s101, s87, 0x30003
	s_lshr_b32 s99, s98, 2
	s_and_b32 s100, s98, 3
	s_lshl_b32 s100, s100, 3
	s_or_b32 s99, s99, s100
	v_and_b32_e32 v2, 63, v0
	v_lshlrev_b32_e32 v3, 2, v2
	v_add_u32_e32 v3, 0x23c00, v3
	v_mov_b32_e32 v4, 0x7fff0000
	ds_write_b32 v3, v4
	v_min_u32_e32 v5, 31, v2
	v_lshlrev_b32_e32 v5, 2, v5
	v_add_u32_e32 v5, 0x22020, v5
	ds_read2_b32 v[6:7], v5 offset1:1
	s_waitcnt lgkmcnt(0)
	v_sub_u32_e32 v8, v7, v6
	v_add_u32_e32 v9, -1, v7
	v_max_i32_e32 v9, 0, v9
	v_lshlrev_b32_e32 v9, 2, v9
	v_add_u32_e32 v9, 0x22400, v9
	ds_read_b32 v9, v9
	s_waitcnt lgkmcnt(0)
	v_cmp_gt_i32_e32 vcc, 0x81, v9
	v_cmp_lt_i32_e64 s[10:11], 0, v8
	s_and_b64 vcc, vcc, s[10:11]
	v_cmp_gt_u32_e64 s[10:11], 32, v2
	s_and_b64 vcc, vcc, s[10:11]
	v_cndmask_b32_e64 v10, 0, 1, vcc
	v_cndmask_b32_e64 v8, 0, v8, s[10:11]
	v_sub_u32_e32 v11, v8, v10
	v_lshl_or_b32 v13, v10, 16, v11
	s_nop 1
	v_add_u32_dpp v13, v13, v13 row_shr:1 row_mask:0xf bank_mask:0xf bound_ctrl:0
	s_nop 1
	v_add_u32_dpp v13, v13, v13 row_shr:2 row_mask:0xf bank_mask:0xf bound_ctrl:0
	s_nop 1
	v_add_u32_dpp v13, v13, v13 row_shr:4 row_mask:0xf bank_mask:0xf bound_ctrl:0
	s_nop 1
	v_add_u32_dpp v13, v13, v13 row_shr:8 row_mask:0xf bank_mask:0xf bound_ctrl:0
	s_nop 1
	v_add_u32_dpp v13, v13, v13 row_bcast:15 row_mask:0xa bank_mask:0xf
	s_nop 1
	v_and_b32_e32 v14, 0xffff, v13
	v_sub_u32_e32 v14, v14, v11
	v_lshrrev_b32_e32 v15, 16, v13
	v_sub_u32_e32 v15, v15, v10
	v_add_u32_e32 v16, v14, v11
	v_add_u32_e32 v17, -1, v8
	s_mov_b32 s12, 0
	s_mov_b64 s[8:9], exec
.Lsch8_loop:
	s_mov_b64 exec, s[8:9]
	v_cmp_lt_i32_e32 vcc, s12, v8
	s_and_b64 exec, exec, vcc
	s_cbranch_execz .Lsch8_end
	v_cmp_eq_u32_e32 vcc, s12, v17
	v_cmp_eq_u32_e64 s[10:11], 1, v10
	s_and_b64 vcc, vcc, s[10:11]
	v_add_u32_e32 v3, s12, v14
	v_cndmask_b32_e32 v4, v3, v15, vcc
	v_cndmask_b32_e32 v5, v15, v16, vcc
	v_mov_b32_e32 v7, s98
	v_mov_b32_e32 v9, s99
	v_cndmask_b32_e32 v12, v7, v9, vcc
	v_cndmask_b32_e32 v7, v9, v7, vcc
	v_and_b32_e32 v9, 31, v4
	v_cmp_eq_u32_e32 vcc, v9, v12
	v_lshrrev_b32_e32 v4, 5, v4
	v_add_u32_e32 v5, 31, v5
	v_sub_u32_e32 v5, v5, v7
	v_lshrrev_b32_e32 v5, 5, v5
	v_add_u32_e32 v4, v4, v5
	v_lshlrev_b32_e32 v4, 2, v4
	v_add_u32_e32 v4, 0x23c00, v4
	v_add_u32_e32 v5, s12, v6
	v_lshl_or_b32 v5, v5, 3, s101
	s_and_b64 exec, exec, vcc
	ds_write_b32 v4, v5
	s_add_i32 s12, s12, 1
	s_branch .Lsch8_loop

; #define LAS __attribute__((address_space(3)))
; #define PG8_STAGE(bufoff, gbase, voff) do { _Pragma("unroll") for (int _i = 0; _i < 2; ++_i) \
;         __builtin_amdgcn_global_load_lds((const unsigned*)((const char*)(gbase) + (voff)[_i]), (LAS unsigned*)(lds + (bufoff) + ldsw + _i * 8192), 16, 0, 0); } while (0)
; #define PG8_WAIT_V(n) asm volatile("s_waitcnt vmcnt(" #n ")" ::: "memory")
; template <class Epi, class Sched, bool GATHER, bool FP8>
; __device__ __forceinline__ void gemm_phase(LAS uchar* lds, const int K, const int LDA, const int LDB, const size_t kstepA, const size_t kstepB, const Sched& S, const Epi& E) {
;     ...
;     Unit cur, nxt; int ui = 0;
;     if (!S.next(0, cur)) return;
;     f32x4 acc[2][2][4][2];
; #pragma unroll
;     for (int a = 0; a < 2; ++a)
; #pragma unroll
;         for (int b = 0; b < 2; ++b)
; #pragma unroll
;             for (int m = 0; m < 4; ++m)
; #pragma unroll
;                 for (int n = 0; n < 2; ++n) acc[a][b][m][n] = (f32x4){0.f, 0.f, 0.f, 0.f};
;     bf16x8 At[4][2], B0[2][2], B1[2][2];
;     const char* cA = cur.pa; const char* cB = cur.pb;
;     if constexpr (GATHER) S.gather(cur, voA, (const LAS int*)nullptr);
;     PG8_STAGE(PG8_SB(0, 0), cB, voffB); PG8_STAGE(PG8_SB(0, 1), cB + hstep, voffB); PG8_STAGE(PG8_SA(0, 0), cA, voA[0]); PG8_STAGE(PG8_SA(0, 1), cA, voA[1]);
;     if (wr == 1) PG8_BAR;
;     PG8_WAIT_V(2); PG8_BAR;
;     PG8_STAGE(PG8_SB(1, 0), cB + kstepB, voffB); PG8_STAGE(PG8_SA(1, 0), cA + kstepA, voA[0]); PG8_STAGE(PG8_SB(1, 1), cB + hstep + kstepB, voffB);
;     __device__ __forceinline__ bool next(int i, pg8::Unit& u) const {
;         const int NB = __builtin_amdgcn_readfirstlane(tab[0]); const int L = i * G + c; if (L >= NB * nN) return false;
;         const int b = L / nN, pn = L - b * nN, e = __builtin_amdgcn_readfirstlane(tab[64 + b]);
;         u.pa = A; u.pb = B + (size_t)e * bexp + (size_t)pn * 256 * 128; u.row0 = b * 256; u.col0 = pn * 256; u.aux = e; u.blk = b; return true;
;     }
;     __device__ __forceinline__ void gather(const pg8::Unit& u, unsigned (&vo)[2][2], const LAS int*) const {
; #pragma unroll
;         for (int i = 0; i < 2; ++i) { int R, C; pg8::stage_rc((int)threadIdx.x * 16 + i * 8192, R, C);
; #pragma unroll
;             for (int h = 0; h < 2; ++h) vo[h][i] = (unsigned)(u.row0 + h * 128 + R) * (unsigned)W8LD + (unsigned)C * 2u; }
;     }
.Lsch8_done:
	s_barrier
	s_add_i32 s4, 0, 0x22000
	v_mov_b32_e32 v2, s4
	ds_read_b32 v2, v2
	v_readfirstlane_b32 s18, v0
	s_waitcnt lgkmcnt(0)
	v_readfirstlane_b32 s4, v2
	s_lshl_b32 s4, s4, 3
	v_mov_b32_e32 v3, 0x23c00
	ds_read_b32 v3, v3
	s_waitcnt lgkmcnt(0)
	v_readfirstlane_b32 s98, v3
	s_cmp_ge_i32 s98, s4
	s_cbranch_scc1 .LBB0_1041
	v_lshlrev_b32_e32 v3, 4, v0
	v_and_b32_e32 v2, 32, v0
	v_bitop3_b32 v2, v3, v2, 48 bitop3:0x6c
	v_or_b32_e32 v3, 0x2000, v3
	v_bfe_u32 v5, v0, 2, 4
	v_lshrrev_b32_e32 v6, 7, v3
	s_movk_i32 s8, 0x70
	s_add_u32 s4, s90, 0x1c000000
	v_and_or_b32 v216, v6, s8, v5
	v_lshrrev_b32_e32 v6, 5, v0
	s_addc_u32 s5, s91, 0
	v_and_or_b32 v195, v0, 64, v2
	v_and_b32_e32 v2, 48, v0
	v_and_b32_e32 v6, 4, v6
	v_bfe_u32 v7, v0, 2, 2
	s_add_u32 s23, s90, 0x50000000
	v_or3_b32 v6, v7, v6, v2
	v_lshrrev_b32_e32 v3, 6, v3
	s_movk_i32 s8, 0xc0
	s_addc_u32 s33, s91, 0
	v_and_or_b32 v3, v3, s8, v6
	s_ashr_i32 s8, s98, 31
	s_lshr_b32 s8, s8, 29
	s_add_i32 s8, s98, s8
	s_ashr_i32 s10, s8, 3
	s_lshl_b32 s9, s10, 2
	s_add_i32 s9, s9, 0
	s_add_i32 s9, s9, 0x22100
	v_lshl_or_b32 v196, v3, 7, v195
	v_mov_b32_e32 v3, s9
	ds_read_b32 v3, v3
	s_lshr_b32 s16, s18, 6
	s_and_b32 s8, s8, -8
	s_lshr_b32 s17, s18, 8
	s_lshl_b32 s44, s16, 10
	s_waitcnt lgkmcnt(0)
	v_readfirstlane_b32 s34, v3
	s_ashr_i32 s35, s34, 31
	s_sub_i32 s14, s98, s8
	s_lshl_b64 s[8:9], s[34:35], 22
	s_add_u32 s11, s23, s8
	s_addc_u32 s12, s33, s9
	s_ashr_i32 s15, s14, 31
	s_lshl_b64 s[8:9], s[14:15], 15
	v_lshrrev_b32_e32 v4, 2, v0
	s_add_u32 s36, s11, s8
	v_and_or_b32 v4, v4, 64, v6
	s_addc_u32 s37, s12, s9
	s_lshl_b32 s69, s10, 8
	v_lshl_or_b32 v198, v4, 7, v195
	s_movk_i32 s45, 0x80
	v_or_b32_e32 v4, s69, v216
	v_mul_lo_u32 v4, v4, s45
	v_or_b32_e32 v219, 0x80, v216
	s_add_i32 s46, s44, 0
	v_or_b32_e32 v202, v4, v195
	v_or_b32_e32 v4, s69, v219
	s_add_i32 s47, s46, 0x10000
	v_mov_b32_e32 v201, 0
	v_lshrrev_b32_e32 v3, 3, v0
	v_mul_lo_u32 v4, v4, s45
	v_mov_b32_e32 v199, v201
	s_mov_b32 m0, s47
	s_add_i32 s48, s46, 0x12000
	v_and_or_b32 v217, v3, 48, v5
	v_or_b32_e32 v204, v4, v195
	v_lshl_add_u64 v[4:5], s[36:37], 0, v[198:199]
	global_load_lds_dwordx4 v198, s[36:37]
	v_mov_b32_e32 v197, v201
	s_mov_b32 m0, s48
	s_add_i32 s49, s46, 0x14000
	s_mov_b64 s[8:9], 0x400
	v_or_b32_e32 v3, s69, v217
	v_lshl_add_u64 v[6:7], s[36:37], 0, v[196:197]
	global_load_lds_dwordx4 v196, s[36:37]
	v_lshl_add_u64 v[4:5], v[4:5], 0, s[8:9]
	s_mov_b32 m0, s49
	s_add_i32 s50, s46, 0x16000
	v_mul_lo_u32 v3, v3, s45
	v_or_b32_e32 v218, 0x80, v217
	global_load_lds_dwordx4 v[4:5], off
	v_lshl_add_u64 v[4:5], v[6:7], 0, s[8:9]
	s_mov_b32 m0, s50
	v_or_b32_e32 v200, v3, v195
	v_or_b32_e32 v3, s69, v218
	global_load_lds_dwordx4 v[4:5], off
	s_mov_b32 m0, s46
	s_add_i32 s51, s46, 0x2000
	v_mul_lo_u32 v3, v3, s45
	global_load_lds_dwordx4 v200, s[4:5]
	s_mov_b32 m0, s51
	s_add_i32 s52, s46, 0x4000
	v_or_b32_e32 v3, v3, v195
	global_load_lds_dwordx4 v202, s[4:5]
	s_mov_b32 m0, s52
	s_add_i32 s53, s46, 0x6000
	global_load_lds_dwordx4 v3, s[4:5]
	s_mov_b32 m0, s53
	s_load_dwordx2 s[10:11], s[0:1], 0x88
	global_load_lds_dwordx4 v204, s[4:5]
	s_cmp_eq_u32 s17, 1
	s_mov_b32 s54, 0x10000
	s_cselect_b64 s[12:13], -1, 0
	s_cmp_lg_u32 s17, 1
	v_mov_b32_e32 v203, v201
	s_cbranch_scc1 .LBB0_1025
	s_barrier

; template <class Epi, class Sched, bool GATHER, bool FP8>
; __device__ __forceinline__ void gemm_phase(LAS uchar* lds, const int K, const int LDA, const int LDB, const size_t kstepA, const size_t kstepB, const Sched& S, const Epi& E) {
;     ...
;         const bool has_next = S.next(ui + 1, nxt);
;         if constexpr (GATHER) { if (has_next) S.prefetch(nxt, lds + LDS_IDX + ((ui + 1) & 1) * 1024, wid, lane); }
;         E.prefetch(cur, lds + LDS_BIAS + (ui & 1) * 1024, wid, lane);
;         const char* nA = has_next ? nxt.pa : cA; const char* nB = has_next ? nxt.pb : cB;
;     __device__ __forceinline__ bool next(int i, pg8::Unit& u) const {
;         const int NB = __builtin_amdgcn_readfirstlane(tab[0]); const int L = i * G + c; if (L >= NB * nN) return false;
;         const int b = L / nN, pn = L - b * nN, e = __builtin_amdgcn_readfirstlane(tab[64 + b]);
;         u.pa = A; u.pb = B + (size_t)e * bexp + (size_t)pn * 256 * 128; u.row0 = b * 256; u.col0 = pn * 256; u.aux = e; u.blk = b; return true;
.LBB0_1028:
	s_lshr_b32 s99, s69, 6
	s_add_i32 s99, s99, 0x22400
	v_mov_b32_e32 v250, s99
	ds_read_b32 v250, v250
	s_lshr_b32 s101, s93, 2
	s_lshl_b32 s101, s101, 6
	s_waitcnt lgkmcnt(0)
	v_readfirstlane_b32 s99, v250
	s_cmp_le_i32 s99, s101
	s_cselect_b32 s100, 1, 0
	s_add_i32 s101, s101, 0x80
	s_cmp_le_i32 s99, s101
	s_cselect_b32 s99, 2, 0
	s_or_b32 s99, s99, s100
	ds_read_b32 v2, v221
	s_add_i32 s67, s38, 1
	s_lshl_b32 s31, s67, 2
	s_add_i32 s31, s31, 0x23c00
	v_mov_b32_e32 v249, s31
	ds_read_b32 v249, v249
	s_waitcnt lgkmcnt(0)
	v_readfirstlane_b32 s28, v2
	s_lshl_b32 s35, s28, 3
	v_readfirstlane_b32 s31, v249
	s_cmp_lt_i32 s31, s35
	s_cselect_b64 s[28:29], -1, 0
	s_cmp_ge_i32 s31, s35
	s_cbranch_scc1 .LBB0_1030
	s_ashr_i32 s24, s31, 31
	s_lshr_b32 s24, s24, 29
	s_add_i32 s24, s31, s24
	s_ashr_i32 s35, s24, 3
	s_lshl_b32 s25, s35, 2
	s_add_i32 s25, s25, 0
	s_add_i32 s25, s25, 0x22100
	v_mov_b32_e32 v2, s25
	ds_read_b32 v2, v2
	s_and_b32 s24, s24, -8
	s_sub_i32 s40, s31, s24
	s_waitcnt lgkmcnt(0)
	v_readfirstlane_b32 s24, v2
	s_ashr_i32 s25, s24, 31
	s_lshl_b64 s[26:27], s[24:25], 22
	s_add_u32 s25, s23, s26
	s_addc_u32 s31, s33, s27
	s_ashr_i32 s41, s40, 31
	s_lshl_b64 s[26:27], s[40:41], 15
	s_add_u32 s26, s25, s26
	s_addc_u32 s27, s31, s27
	s_lshl_b32 s68, s35, 8
	s_lshl_b32 s25, s40, 8

; #define PG8_STAGE(bufoff, gbase, voff) do { _Pragma("unroll") for (int _i = 0; _i < 2; ++_i) \
;         __builtin_amdgcn_global_load_lds((const unsigned*)((const char*)(gbase) + (voff)[_i]), (LAS unsigned*)(lds + (bufoff) + ldsw + _i * 8192), 16, 0, 0); } while (0)
; #define PG8_LDA(dst, b, h) do { _Pragma("unroll") for (int m = 0; m < 4; ++m) _Pragma("unroll") for (int k = 0; k < 2; ++k) dst[m][k] = *(const LAS bf16x8*)(lds + PG8_SA(b, h) + aoff + m * 2048 + k * 1024); } while (0)
; #define PG8_WAIT_V8F(fresh) asm volatile("s_cmp_eq_u32 %0, 0\n\ts_cbranch_scc1 .Lw8_%=\n\ts_waitcnt vmcnt(%1)\n\ts_branch .Lwe_%=\n.Lw8_%=:\n\ts_waitcnt vmcnt(8)\n.Lwe_%=:" :: "s"(fresh), "n"(8 + Epi::NST + Epi::NPF) : "memory", "scc")
; #define PG8_WAIT_L(n) asm volatile("s_waitcnt lgkmcnt(" #n ")" ::: "memory")
; #define PG8_BAR __builtin_amdgcn_s_barrier()
; #define PG8_SCHED __builtin_amdgcn_sched_barrier(0)
; template <class Epi, class Sched, bool GATHER, bool FP8>
; __device__ __forceinline__ void gemm_phase(LAS uchar* lds, const int K, const int LDA, const int LDB, const size_t kstepA, const size_t kstepB, const Sched& S, const Epi& E) {
;     ...
;             PG8_WAIT_V8F(fresh); PG8_WAIT_L(0); PG8_BAR; PG8_MMA(0, 0, At, B0); PG8_MMA(0, 1, At, B1); PG8_BAR; PG8_SCHED;
;             PG8_LDA(At, 0, 1); PG8_STAGE(PG8_SB(0, 0), b2, voffB); PG8_STAGE(PG8_SB(0, 1), b2 + hstep, voffB); PG8_STAGE(PG8_SA(0, 0), a2, voA[0]);
.Lwe_6:
	s_waitcnt lgkmcnt(0)
	s_barrier
	s_setprio 1
	s_waitcnt lgkmcnt(0)
	s_bitcmp1_b32 s99, 0
	s_cbranch_scc1 .Lmsk8_0
	v_mfma_scale_f32_16x16x128_f8f6f4 v[190:193], v[18:25], v[58:65], v[190:193], v226, v226 op_sel_hi:[0,0,0]
	v_mfma_scale_f32_16x16x128_f8f6f4 v[186:189], v[26:33], v[58:65], v[186:189], v226, v226 op_sel_hi:[0,0,0]
	v_mfma_scale_f32_16x16x128_f8f6f4 v[174:177], v[18:25], v[50:57], v[174:177], v226, v226 op_sel_hi:[0,0,0]
	v_mfma_scale_f32_16x16x128_f8f6f4 v[170:173], v[26:33], v[50:57], v[170:173], v226, v226 op_sel_hi:[0,0,0]
	v_mfma_scale_f32_16x16x128_f8f6f4 v[158:161], v[18:25], v[42:49], v[158:161], v226, v226 op_sel_hi:[0,0,0]
	v_mfma_scale_f32_16x16x128_f8f6f4 v[154:157], v[26:33], v[42:49], v[154:157], v226, v226 op_sel_hi:[0,0,0]
	v_mfma_scale_f32_16x16x128_f8f6f4 v[142:145], v[18:25], v[34:41], v[142:145], v226, v226 op_sel_hi:[0,0,0]
	v_mfma_scale_f32_16x16x128_f8f6f4 v[138:141], v[26:33], v[34:41], v[138:141], v226, v226 op_sel_hi:[0,0,0]
	s_setprio 0
	s_setprio 1
	v_mfma_scale_f32_16x16x128_f8f6f4 v[182:185], v[2:9], v[58:65], v[182:185], v226, v226 op_sel_hi:[0,0,0]
	v_mfma_scale_f32_16x16x128_f8f6f4 v[178:181], v[10:17], v[58:65], v[178:181], v226, v226 op_sel_hi:[0,0,0]
	v_mfma_scale_f32_16x16x128_f8f6f4 v[166:169], v[2:9], v[50:57], v[166:169], v226, v226 op_sel_hi:[0,0,0]
	v_mfma_scale_f32_16x16x128_f8f6f4 v[162:165], v[10:17], v[50:57], v[162:165], v226, v226 op_sel_hi:[0,0,0]
	v_mfma_scale_f32_16x16x128_f8f6f4 v[150:153], v[2:9], v[42:49], v[150:153], v226, v226 op_sel_hi:[0,0,0]
	v_mfma_scale_f32_16x16x128_f8f6f4 v[146:149], v[10:17], v[42:49], v[146:149], v226, v226 op_sel_hi:[0,0,0]
	v_mfma_scale_f32_16x16x128_f8f6f4 v[134:137], v[2:9], v[34:41], v[134:137], v226, v226 op_sel_hi:[0,0,0]
	v_mfma_scale_f32_16x16x128_f8f6f4 v[130:133], v[10:17], v[34:41], v[130:133], v226, v226 op_sel_hi:[0,0,0]
.Lmsk8_0:
	s_setprio 0
	s_barrier
	s_mov_b32 m0, s47
	v_lshl_add_u64 v[230:231], s[38:39], 0, v[198:199]
	ds_read_b128 v[34:37], v225 offset:16384
	ds_read_b128 v[38:41], v225 offset:17408
	ds_read_b128 v[42:45], v225 offset:18432
	ds_read_b128 v[46:49], v225 offset:19456
	ds_read_b128 v[50:53], v225 offset:20480
	ds_read_b128 v[54:57], v225 offset:21504
	ds_read_b128 v[58:61], v225 offset:22528
	ds_read_b128 v[62:65], v225 offset:23552
	global_load_lds_dwordx4 v[230:231], off
	v_lshl_add_u64 v[232:233], s[38:39], 0, v[196:197]
	s_mov_b32 m0, s48
	v_lshl_add_u64 v[230:231], v[230:231], 0, s[8:9]
	global_load_lds_dwordx4 v[232:233], off
	s_mov_b32 m0, s49
	v_mov_b32_e32 v207, v201
	global_load_lds_dwordx4 v[230:231], off
	v_lshl_add_u64 v[230:231], v[232:233], 0, s[8:9]
	s_mov_b32 m0, s50
	v_mov_b32_e32 v203, v201
	global_load_lds_dwordx4 v[230:231], off
	s_mov_b32 m0, s46
	v_lshl_add_u64 v[230:231], s[42:43], 0, v[206:207]
	global_load_lds_dwordx4 v206, s[42:43]
	s_mov_b32 m0, s51
	v_lshl_add_u64 v[232:233], s[42:43], 0, v[202:203]
	global_load_lds_dwordx4 v202, s[42:43]
	s_cmp_eq_u32 s73, 0
	s_cbranch_scc1 .Lw8_7
	s_waitcnt vmcnt(17)
	s_branch .Lwe_7

; #define PG8_STAGE(bufoff, gbase, voff) do { _Pragma("unroll") for (int _i = 0; _i < 2; ++_i) \
;         __builtin_amdgcn_global_load_lds((const unsigned*)((const char*)(gbase) + (voff)[_i]), (LAS unsigned*)(lds + (bufoff) + ldsw + _i * 8192), 16, 0, 0); } while (0)
; #define PG8_LDA(dst, b, h) do { _Pragma("unroll") for (int m = 0; m < 4; ++m) _Pragma("unroll") for (int k = 0; k < 2; ++k) dst[m][k] = *(const LAS bf16x8*)(lds + PG8_SA(b, h) + aoff + m * 2048 + k * 1024); } while (0)
; #define PG8_LDB(dst, b, h) do { _Pragma("unroll") for (int n = 0; n < 2; ++n) _Pragma("unroll") for (int k = 0; k < 2; ++k) dst[n][k] = *(const LAS bf16x8*)(lds + PG8_SB(b, h) + boff + n * 2048 + k * 1024); } while (0)
; #define PG8_WAIT_V(n) asm volatile("s_waitcnt vmcnt(" #n ")" ::: "memory")
; #define PG8_WAIT_V8F(fresh) asm volatile("s_cmp_eq_u32 %0, 0\n\ts_cbranch_scc1 .Lw8_%=\n\ts_waitcnt vmcnt(%1)\n\ts_branch .Lwe_%=\n.Lw8_%=:\n\ts_waitcnt vmcnt(8)\n.Lwe_%=:" :: "s"(fresh), "n"(8 + Epi::NST + Epi::NPF) : "memory", "scc")
; #define PG8_WAIT_L(n) asm volatile("s_waitcnt lgkmcnt(" #n ")" ::: "memory")
; #define PG8_BAR __builtin_amdgcn_s_barrier()
; #define PG8_SCHED __builtin_amdgcn_sched_barrier(0)
; template <class Epi, class Sched, bool GATHER, bool FP8>
; __device__ __forceinline__ void gemm_phase(LAS uchar* lds, const int K, const int LDA, const int LDB, const size_t kstepA, const size_t kstepB, const Sched& S, const Epi& E) {
;     ...
;             PG8_WAIT_V8F(fresh); PG8_WAIT_L(0); PG8_BAR; PG8_MMA(1, 0, At, B0); PG8_MMA(1, 1, At, B1); PG8_BAR; PG8_SCHED;
;             PG8_LDB(B0, 1, 0); PG8_LDB(B1, 1, 1); PG8_SCHED; PG8_LDA(At, 1, 0); PG8_STAGE(PG8_SA(0, 1), a2, voA[1]);
;             PG8_WAIT_V(8); PG8_WAIT_L(0); PG8_BAR; PG8_MMA(0, 0, At, B0); PG8_MMA(0, 1, At, B1); PG8_BAR; PG8_SCHED;
.Lwe_7:
	s_waitcnt lgkmcnt(0)
	s_barrier
	s_setprio 1
	s_waitcnt lgkmcnt(0)
	s_bitcmp1_b32 s99, 1
	s_cbranch_scc1 .Lmsk8_1
	v_mfma_scale_f32_16x16x128_f8f6f4 v[126:129], v[18:25], v[34:41], v[126:129], v226, v226 op_sel_hi:[0,0,0]
	v_mfma_scale_f32_16x16x128_f8f6f4 v[122:125], v[26:33], v[34:41], v[122:125], v226, v226 op_sel_hi:[0,0,0]
	v_mfma_scale_f32_16x16x128_f8f6f4 v[110:113], v[18:25], v[42:49], v[110:113], v226, v226 op_sel_hi:[0,0,0]
	v_mfma_scale_f32_16x16x128_f8f6f4 v[106:109], v[26:33], v[42:49], v[106:109], v226, v226 op_sel_hi:[0,0,0]
	v_mfma_scale_f32_16x16x128_f8f6f4 v[94:97], v[18:25], v[50:57], v[94:97], v226, v226 op_sel_hi:[0,0,0]
	v_mfma_scale_f32_16x16x128_f8f6f4 v[90:93], v[26:33], v[50:57], v[90:93], v226, v226 op_sel_hi:[0,0,0]
	v_mfma_scale_f32_16x16x128_f8f6f4 v[78:81], v[18:25], v[58:65], v[78:81], v226, v226 op_sel_hi:[0,0,0]
	v_mfma_scale_f32_16x16x128_f8f6f4 v[74:77], v[26:33], v[58:65], v[74:77], v226, v226 op_sel_hi:[0,0,0]
	s_setprio 0
	s_setprio 1
	v_mfma_scale_f32_16x16x128_f8f6f4 v[118:121], v[2:9], v[34:41], v[118:121], v226, v226 op_sel_hi:[0,0,0]
	v_mfma_scale_f32_16x16x128_f8f6f4 v[114:117], v[10:17], v[34:41], v[114:117], v226, v226 op_sel_hi:[0,0,0]
	v_mfma_scale_f32_16x16x128_f8f6f4 v[102:105], v[2:9], v[42:49], v[102:105], v226, v226 op_sel_hi:[0,0,0]
	v_mfma_scale_f32_16x16x128_f8f6f4 v[98:101], v[10:17], v[42:49], v[98:101], v226, v226 op_sel_hi:[0,0,0]
	v_mfma_scale_f32_16x16x128_f8f6f4 v[86:89], v[2:9], v[50:57], v[86:89], v226, v226 op_sel_hi:[0,0,0]
	v_mfma_scale_f32_16x16x128_f8f6f4 v[82:85], v[10:17], v[50:57], v[82:85], v226, v226 op_sel_hi:[0,0,0]
	v_mfma_scale_f32_16x16x128_f8f6f4 v[70:73], v[2:9], v[58:65], v[70:73], v226, v226 op_sel_hi:[0,0,0]
	v_mfma_scale_f32_16x16x128_f8f6f4 v[66:69], v[10:17], v[58:65], v[66:69], v226, v226 op_sel_hi:[0,0,0]
.Lmsk8_1:
	s_setprio 0
	s_barrier
	s_add_i32 s73, 0, 0x18000
	s_add_i32 s74, 0, 0x1c000
	v_add_u32_e32 v14, s73, v220
	v_add_u32_e32 v30, s74, v220
	ds_read_b128 v[2:5], v14
	ds_read_b128 v[6:9], v14 offset:1024
	ds_read_b128 v[10:13], v14 offset:2048
	ds_read_b128 v[14:17], v14 offset:3072
	ds_read_b128 v[18:21], v30
	ds_read_b128 v[22:25], v30 offset:1024
	ds_read_b128 v[26:29], v30 offset:2048
	ds_read_b128 v[30:33], v30 offset:3072
	s_mov_b32 m0, s52
	v_lshl_add_u64 v[214:215], s[42:43], 0, v[214:215]
	ds_read_b128 v[34:37], v225 offset:32768
	ds_read_b128 v[38:41], v225 offset:33792
	ds_read_b128 v[42:45], v225 offset:34816
	ds_read_b128 v[46:49], v225 offset:35840
	ds_read_b128 v[50:53], v225 offset:36864
	ds_read_b128 v[54:57], v225 offset:37888
	ds_read_b128 v[58:61], v225 offset:38912
	ds_read_b128 v[62:65], v225 offset:39936
	global_load_lds_dwordx4 v[214:215], off
	v_lshl_add_u64 v[212:213], s[42:43], 0, v[212:213]
	s_mov_b32 m0, s53
	s_nop 0
	global_load_lds_dwordx4 v[212:213], off
	s_waitcnt vmcnt(8)
	s_waitcnt lgkmcnt(0)
	s_barrier
	s_setprio 1
	s_waitcnt lgkmcnt(0)
	s_bitcmp1_b32 s99, 0
	s_cbranch_scc1 .Lmsk8_2
	v_mfma_scale_f32_16x16x128_f8f6f4 v[190:193], v[2:9], v[34:41], v[190:193], v226, v226 op_sel_hi:[0,0,0]
	v_mfma_scale_f32_16x16x128_f8f6f4 v[186:189], v[10:17], v[34:41], v[186:189], v226, v226 op_sel_hi:[0,0,0]
	v_mfma_scale_f32_16x16x128_f8f6f4 v[174:177], v[2:9], v[42:49], v[174:177], v226, v226 op_sel_hi:[0,0,0]
	v_mfma_scale_f32_16x16x128_f8f6f4 v[170:173], v[10:17], v[42:49], v[170:173], v226, v226 op_sel_hi:[0,0,0]
	v_mfma_scale_f32_16x16x128_f8f6f4 v[158:161], v[2:9], v[50:57], v[158:161], v226, v226 op_sel_hi:[0,0,0]
	v_mfma_scale_f32_16x16x128_f8f6f4 v[154:157], v[10:17], v[50:57], v[154:157], v226, v226 op_sel_hi:[0,0,0]
	v_mfma_scale_f32_16x16x128_f8f6f4 v[142:145], v[2:9], v[58:65], v[142:145], v226, v226 op_sel_hi:[0,0,0]
	v_mfma_scale_f32_16x16x128_f8f6f4 v[138:141], v[10:17], v[58:65], v[138:141], v226, v226 op_sel_hi:[0,0,0]
	s_setprio 0
	s_setprio 1
	v_mfma_scale_f32_16x16x128_f8f6f4 v[182:185], v[18:25], v[34:41], v[182:185], v226, v226 op_sel_hi:[0,0,0]
	v_mfma_scale_f32_16x16x128_f8f6f4 v[178:181], v[26:33], v[34:41], v[178:181], v226, v226 op_sel_hi:[0,0,0]
	v_mfma_scale_f32_16x16x128_f8f6f4 v[166:169], v[18:25], v[42:49], v[166:169], v226, v226 op_sel_hi:[0,0,0]
	v_mfma_scale_f32_16x16x128_f8f6f4 v[162:165], v[26:33], v[42:49], v[162:165], v226, v226 op_sel_hi:[0,0,0]
	v_mfma_scale_f32_16x16x128_f8f6f4 v[150:153], v[18:25], v[50:57], v[150:153], v226, v226 op_sel_hi:[0,0,0]
	v_mfma_scale_f32_16x16x128_f8f6f4 v[146:149], v[26:33], v[50:57], v[146:149], v226, v226 op_sel_hi:[0,0,0]
	v_mfma_scale_f32_16x16x128_f8f6f4 v[134:137], v[18:25], v[58:65], v[134:137], v226, v226 op_sel_hi:[0,0,0]
	v_mfma_scale_f32_16x16x128_f8f6f4 v[130:133], v[26:33], v[58:65], v[130:133], v226, v226 op_sel_hi:[0,0,0]
; #define PG8_STAGE(bufoff, gbase, voff) do { _Pragma("unroll") for (int _i = 0; _i < 2; ++_i) \
;         __builtin_amdgcn_global_load_lds((const unsigned*)((const char*)(gbase) + (voff)[_i]), (LAS unsigned*)(lds + (bufoff) + ldsw + _i * 8192), 16, 0, 0); } while (0)
; #define PG8_LDA(dst, b, h) do { _Pragma("unroll") for (int m = 0; m < 4; ++m) _Pragma("unroll") for (int k = 0; k < 2; ++k) dst[m][k] = *(const LAS bf16x8*)(lds + PG8_SA(b, h) + aoff + m * 2048 + k * 1024); } while (0)
; #define PG8_WAIT_V8F(fresh) asm volatile("s_cmp_eq_u32 %0, 0\n\ts_cbranch_scc1 .Lw8_%=\n\ts_waitcnt vmcnt(%1)\n\ts_branch .Lwe_%=\n.Lw8_%=:\n\ts_waitcnt vmcnt(8)\n.Lwe_%=:" :: "s"(fresh), "n"(8 + Epi::NST + Epi::NPF) : "memory", "scc")
; #define PG8_WAIT_L(n) asm volatile("s_waitcnt lgkmcnt(" #n ")" ::: "memory")
; #define PG8_BAR __builtin_amdgcn_s_barrier()
; #define PG8_SCHED __builtin_amdgcn_sched_barrier(0)
; template <class Epi, class Sched, bool GATHER, bool FP8>
; __device__ __forceinline__ void gemm_phase(LAS uchar* lds, const int K, const int LDA, const int LDB, const size_t kstepA, const size_t kstepB, const Sched& S, const Epi& E) {
;     ...
;             PG8_LDA(At, 0, 1); PG8_STAGE(PG8_SB(0, 0), b2, voffB); PG8_STAGE(PG8_SB(0, 1), b2 + hstep, voffB); PG8_STAGE(PG8_SA(0, 0), a2, voA[0]);
;             PG8_WAIT_V8F(fresh); PG8_WAIT_L(0); PG8_BAR; PG8_MMA(1, 0, At, B0); PG8_MMA(1, 1, At, B1); PG8_BAR; PG8_SCHED;
.Lmsk8_2:
	s_setprio 0
	s_barrier
	s_add_i32 s42, s73, s44
	v_lshl_add_u64 v[212:213], s[40:41], 0, v[198:199]
	s_mov_b32 m0, s42
	ds_read_b128 v[34:37], v225 offset:49152
	ds_read_b128 v[38:41], v225 offset:50176
	ds_read_b128 v[42:45], v225 offset:51200
	ds_read_b128 v[46:49], v225 offset:52224
	ds_read_b128 v[50:53], v225 offset:53248
	ds_read_b128 v[54:57], v225 offset:54272
	ds_read_b128 v[58:61], v225 offset:55296
	ds_read_b128 v[62:65], v225 offset:56320
	global_load_lds_dwordx4 v[212:213], off
	s_add_i32 m0, s42, 0x2000
	s_add_u32 s38, s38, 0x40400
	v_lshl_add_u64 v[212:213], s[40:41], 0, v[196:197]
	s_addc_u32 s39, s39, 0
	s_add_i32 s40, s74, s44
	global_load_lds_dwordx4 v[212:213], off
	v_lshl_add_u64 v[212:213], s[38:39], 0, v[198:199]
	s_mov_b32 m0, s40
	s_nop 0
	global_load_lds_dwordx4 v[212:213], off
	v_lshl_add_u64 v[212:213], s[38:39], 0, v[196:197]
	s_add_i32 m0, s40, 0x2000
	s_nop 0
	global_load_lds_dwordx4 v[212:213], off
	v_lshl_add_u64 v[212:213], v[230:231], 0, s[20:21]
	s_mov_b32 m0, s56
	s_nop 0
	global_load_lds_dwordx4 v[212:213], off
	v_lshl_add_u64 v[212:213], v[232:233], 0, s[20:21]
	s_mov_b32 m0, s57
	s_nop 0
	global_load_lds_dwordx4 v[212:213], off
	s_waitcnt vmcnt(8)
	s_waitcnt lgkmcnt(0)
	s_barrier
	s_setprio 1
	s_waitcnt lgkmcnt(0)
	s_bitcmp1_b32 s99, 1
	s_cbranch_scc1 .Lmsk8_3
	v_mfma_scale_f32_16x16x128_f8f6f4 v[126:129], v[2:9], v[34:41], v[126:129], v226, v226 op_sel_hi:[0,0,0]
	v_mfma_scale_f32_16x16x128_f8f6f4 v[122:125], v[10:17], v[34:41], v[122:125], v226, v226 op_sel_hi:[0,0,0]
	v_mfma_scale_f32_16x16x128_f8f6f4 v[110:113], v[2:9], v[42:49], v[110:113], v226, v226 op_sel_hi:[0,0,0]
	v_mfma_scale_f32_16x16x128_f8f6f4 v[106:109], v[10:17], v[42:49], v[106:109], v226, v226 op_sel_hi:[0,0,0]
	v_mfma_scale_f32_16x16x128_f8f6f4 v[94:97], v[2:9], v[50:57], v[94:97], v226, v226 op_sel_hi:[0,0,0]
	v_mfma_scale_f32_16x16x128_f8f6f4 v[90:93], v[10:17], v[50:57], v[90:93], v226, v226 op_sel_hi:[0,0,0]
	v_mfma_scale_f32_16x16x128_f8f6f4 v[78:81], v[2:9], v[58:65], v[78:81], v226, v226 op_sel_hi:[0,0,0]
	v_mfma_scale_f32_16x16x128_f8f6f4 v[74:77], v[10:17], v[58:65], v[74:77], v226, v226 op_sel_hi:[0,0,0]
	s_setprio 0
	s_setprio 1
	v_mfma_scale_f32_16x16x128_f8f6f4 v[118:121], v[18:25], v[34:41], v[118:121], v226, v226 op_sel_hi:[0,0,0]
	v_mfma_scale_f32_16x16x128_f8f6f4 v[114:117], v[26:33], v[34:41], v[114:117], v226, v226 op_sel_hi:[0,0,0]
	v_mfma_scale_f32_16x16x128_f8f6f4 v[102:105], v[18:25], v[42:49], v[102:105], v226, v226 op_sel_hi:[0,0,0]
	v_mfma_scale_f32_16x16x128_f8f6f4 v[98:101], v[26:33], v[42:49], v[98:101], v226, v226 op_sel_hi:[0,0,0]
	v_mfma_scale_f32_16x16x128_f8f6f4 v[86:89], v[18:25], v[50:57], v[86:89], v226, v226 op_sel_hi:[0,0,0]
	v_mfma_scale_f32_16x16x128_f8f6f4 v[82:85], v[26:33], v[50:57], v[82:85], v226, v226 op_sel_hi:[0,0,0]
	v_mfma_scale_f32_16x16x128_f8f6f4 v[70:73], v[18:25], v[58:65], v[70:73], v226, v226 op_sel_hi:[0,0,0]
	v_mfma_scale_f32_16x16x128_f8f6f4 v[66:69], v[26:33], v[58:65], v[66:69], v226, v226 op_sel_hi:[0,0,0]
.Lmsk8_3:
	s_setprio 0
	s_barrier
	s_add_i32 s72, s72, 2
	s_add_u32 s36, s36, 0xa00000
	s_addc_u32 s37, s37, 0
	s_add_u32 s31, s31, 0x80000
	s_addc_u32 s71, s71, 0
	s_cmp_gt_u32 s72, 13
	s_cbranch_scc1 .LBB0_1035
